# gemm tail pointer loads hoisted; agg1 degree sort exchanges (xor 4/8) via DPP instead of ds_swizzle; 40 preloaded index slots + swizzle prefetch
# speedup vs baseline: 1.0222x; 1.0045x over previous
.LBB1_69:
	s_and_b64 vcc, exec, s[4:5]
	s_cbranch_vccz .LBB1_79
	v_lshrrev_b32_e32 v2, 2, v0
	s_load_dwordx4 s[4:7], s[0:1], 0x0
	s_load_dwordx2 s[24:25], s[0:1], 0x18
	s_load_dwordx2 s[26:27], s[0:1], 0x20
	v_and_b32_e32 v2, 0x70, v2
	v_and_b32_e32 v1, 15, v0
	v_lshl_or_b32 v35, s2, 7, v2
	v_or_b32_e32 v34, v35, v1
	v_min_u32_e32 v2, 0xc34f, v34
	v_bfe_u32 v40, v0, 4, 2
	v_lshlrev_b32_e32 v36, 9, v2
	v_mov_b32_e32 v37, 0
	s_waitcnt vmcnt(0) lgkmcnt(0)
	v_lshl_add_u64 v[2:3], s[4:5], 0, v[36:37]
	v_lshlrev_b32_e32 v36, 5, v40
	v_lshl_add_u64 v[54:55], v[2:3], 0, v[36:37]
	global_load_dwordx4 v[30:33], v[54:55], off offset:16 nt
	global_load_dwordx4 v[18:21], v[54:55], off nt
	global_load_dwordx4 v[14:17], v[54:55], off offset:144 nt
	global_load_dwordx4 v[10:13], v[54:55], off offset:128 nt
	global_load_dwordx4 v[6:9], v[54:55], off offset:272 nt
	global_load_dwordx4 v[2:5], v[54:55], off offset:256 nt
	v_readfirstlane_b32 s20, v0
	v_lshlrev_b32_e32 v36, 4, v0
	s_lshr_b32 s20, s20, 6
	s_lshl_b32 s20, s20, 10
	s_mov_b32 m0, s20
	v_add_u32_e32 v42, 0x2000, v36
	global_load_lds_dwordx4 v36, s[6:7]
	s_add_i32 s21, s20, 0x2000
	s_mov_b32 m0, s21
	v_add_u32_e32 v43, 0x4000, v36
	global_load_lds_dwordx4 v42, s[6:7]
	s_add_i32 s21, s20, 0x4000
	s_mov_b32 m0, s21
	v_add_u32_e32 v44, 0x6000, v36
	global_load_lds_dwordx4 v43, s[6:7]
	s_add_i32 s21, s20, 0x6000
	s_mov_b32 m0, s21
	v_add_u32_e32 v45, 0x8000, v36
	global_load_lds_dwordx4 v44, s[6:7]
	s_movk_i32 s2, 0x190
	v_cmp_gt_u32_e32 vcc, s2, v0
	s_add_i32 s21, s20, 0x8000
	s_mov_b32 m0, s21
	s_and_saveexec_b64 s[2:3], vcc
	global_load_lds_dwordx4 v45, s[6:7]
	s_or_b64 exec, exec, s[2:3]
	global_load_dwordx4 v[26:29], v[54:55], off offset:400 nt
	global_load_dwordx4 v[22:25], v[54:55], off offset:384 nt
	s_waitcnt vmcnt(2)
	s_mov_b32 s2, 0xc350
	v_cmp_gt_u32_e32 vcc, s2, v35
	s_waitcnt lgkmcnt(0)
	s_barrier
	s_and_saveexec_b64 s[2:3], vcc
	s_cbranch_execz .LBB1_79
	v_lshlrev_b32_e32 v36, 3, v40
	v_mul_u32_u24_e32 v1, 0x110, v1
	v_lshl_add_u32 v37, v36, 1, v1
	ds_read_b128 v[42:45], v37
	v_cvt_pk_f16_f32 v33, v32, v33
	v_cvt_pk_f16_f32 v32, v30, v31
	v_cvt_pk_f16_f32 v31, v20, v21
	v_cvt_pk_f16_f32 v30, v18, v19
	ds_read_b128 v[18:21], v37 offset:64
	v_cvt_pk_f16_f32 v17, v16, v17
	v_cvt_pk_f16_f32 v16, v14, v15
	v_cvt_pk_f16_f32 v15, v12, v13
	v_cvt_pk_f16_f32 v14, v10, v11
	ds_read_b128 v[10:13], v37 offset:128
	ds_read_b128 v[46:49], v37 offset:192
	s_waitcnt lgkmcnt(3)
	v_mfma_f32_16x16x32_f16 v[42:45], v[42:45], v[30:33], 0
	v_cvt_pk_f16_f32 v9, v8, v9
	v_cvt_pk_f16_f32 v8, v6, v7
	v_cvt_pk_f16_f32 v7, v4, v5
	s_waitcnt lgkmcnt(2)
	v_mfma_f32_16x16x32_f16 v[18:21], v[18:21], v[14:17], v[42:45]
	v_cvt_pk_f16_f32 v6, v2, v3
	s_waitcnt vmcnt(0)
	v_cvt_pk_f16_f32 v3, v24, v25
	v_cvt_pk_f16_f32 v2, v22, v23
	s_waitcnt lgkmcnt(1)
	v_mfma_f32_16x16x32_f16 v[10:13], v[10:13], v[6:9], v[18:21]
	ds_read_b128 v[22:25], v37 offset:4416
	v_cvt_pk_f16_f32 v5, v28, v29
	v_cvt_pk_f16_f32 v4, v26, v27
	ds_read_b128 v[18:21], v37 offset:4352
	s_waitcnt lgkmcnt(0)
	v_mfma_f32_16x16x32_f16 v[18:21], v[18:21], v[30:33], 0
	ds_read_b128 v[26:29], v37 offset:4480
	ds_read_b128 v[42:45], v37 offset:8832
	ds_read_b128 v[50:53], v37 offset:17536
	v_mfma_f32_16x16x32_f16 v[18:21], v[22:25], v[14:17], v[18:21]
	ds_read_b128 v[22:25], v37 offset:4544
	ds_read_b128 v[54:57], v37 offset:21888
	v_mov_b32_e32 v35, 0
	s_waitcnt lgkmcnt(4)
	v_mfma_f32_16x16x32_f16 v[18:21], v[26:29], v[6:9], v[18:21]
	ds_read_b128 v[26:29], v37 offset:8704
	v_mov_b32_e32 v62, v35
	v_mov_b32_e32 v63, v35
	s_waitcnt lgkmcnt(2)
	v_mfma_f32_16x16x32_f16 v[18:21], v[22:25], v[2:5], v[18:21]
	ds_read_b128 v[22:25], v37 offset:8768
	s_load_dwordx2 s[2:3], s[0:1], 0x10
	v_lshrrev_b32_e32 v1, 4, v0
	s_waitcnt lgkmcnt(0)
	v_mfma_f32_16x16x32_f16 v[26:29], v[26:29], v[30:33], 0
	v_lshlrev_b64 v[38:39], 7, v[34:35]
	s_nop 1
	v_cvt_pk_fp8_f32 v63, v18, v19
	v_lshlrev_b32_e32 v1, 2, v1
	v_mfma_f32_16x16x32_f16 v[22:25], v[22:25], v[14:17], v[26:29]
	v_lshl_add_u64 v[38:39], s[2:3], 0, v[38:39]
	v_cvt_pk_fp8_f32 v63, v20, v21 op_sel:[0,0,1]
	v_and_b32_e32 v0, 16, v0
	ds_read_b128 v[26:29], v37 offset:8896
	v_mfma_f32_16x16x32_f16 v[22:25], v[42:45], v[6:9], v[22:25]
	ds_read_b128 v[42:45], v37 offset:13056
	v_cmp_lt_u32_e32 vcc, 1, v40
	s_waitcnt lgkmcnt(1)
	v_mfma_f32_16x16x32_f16 v[22:25], v[26:29], v[2:5], v[22:25]
	ds_read_b128 v[26:29], v37 offset:13120
	v_mfma_f32_16x16x32_f16 v[10:13], v[46:49], v[2:5], v[10:13]
	ds_read_b128 v[46:49], v37 offset:13184
	s_waitcnt lgkmcnt(2)
	v_mfma_f32_16x16x32_f16 v[42:45], v[42:45], v[30:33], 0
	s_waitcnt lgkmcnt(1)
	v_mfma_f32_16x16x32_f16 v[26:29], v[26:29], v[14:17], v[42:45]
	s_nop 2
	v_cvt_pk_fp8_f32 v62, v10, v11
	v_cvt_pk_fp8_f32 v62, v12, v13 op_sel:[0,0,1]
	s_nop 0
	ds_read_b128 v[42:45], v37 offset:13248
	s_waitcnt lgkmcnt(1)
	v_mfma_f32_16x16x32_f16 v[26:29], v[46:49], v[6:9], v[26:29]
	ds_read_b128 v[46:49], v37 offset:17408
	v_permlane16_swap_b32_e32 v62, v63
	s_waitcnt lgkmcnt(1)
	v_mfma_f32_16x16x32_f16 v[26:29], v[42:45], v[2:5], v[26:29]
	ds_read_b128 v[42:45], v37 offset:17472
	s_waitcnt lgkmcnt(1)
	v_mfma_f32_16x16x32_f16 v[46:49], v[46:49], v[30:33], 0
	s_waitcnt lgkmcnt(0)
	v_mfma_f32_16x16x32_f16 v[42:45], v[42:45], v[14:17], v[46:49]
	s_nop 5
	ds_read_b128 v[46:49], v37 offset:17600
	v_mfma_f32_16x16x32_f16 v[42:45], v[50:53], v[6:9], v[42:45]
	ds_read_b128 v[50:53], v37 offset:21760
	s_waitcnt lgkmcnt(1)
	v_mfma_f32_16x16x32_f16 v[42:45], v[46:49], v[2:5], v[42:45]
	ds_read_b128 v[46:49], v37 offset:21824
	s_waitcnt lgkmcnt(1)
	v_mfma_f32_16x16x32_f16 v[50:53], v[50:53], v[30:33], 0
	s_waitcnt lgkmcnt(0)
	v_mfma_f32_16x16x32_f16 v[46:49], v[46:49], v[14:17], v[50:53]
	s_nop 5
	ds_read_b128 v[50:53], v37 offset:21952
	v_mfma_f32_16x16x32_f16 v[46:49], v[54:57], v[6:9], v[46:49]
	ds_read_b128 v[54:57], v37 offset:26112
	ds_read_b128 v[58:61], v37 offset:26176
	ds_read_b128 v[10:13], v37 offset:26240
	s_waitcnt lgkmcnt(2)
	v_mfma_f32_16x16x32_f16 v[18:21], v[54:57], v[30:33], 0
	s_waitcnt lgkmcnt(1)
	v_mfma_f32_16x16x32_f16 v[18:21], v[58:61], v[14:17], v[18:21]
	v_mov_b32_e32 v58, v35
	v_cvt_pk_fp8_f32 v58, v42, v43
	v_mov_b32_e32 v59, v35
	v_mfma_f32_16x16x32_f16 v[46:49], v[50:53], v[2:5], v[46:49]
	v_and_b32_e32 v50, 8, v1
	v_mov_b32_e32 v51, v35
	v_lshl_add_u64 v[38:39], v[38:39], 0, v[50:51]
	ds_read_b128 v[50:53], v37 offset:26304
	s_waitcnt lgkmcnt(1)
	v_mfma_f32_16x16x32_f16 v[10:13], v[10:13], v[6:9], v[18:21]
	s_nop 2
	ds_read_b128 v[18:21], v37 offset:30464
	ds_read_b128 v[54:57], v37 offset:30528
	v_mov_b32_e32 v1, v35
	v_lshl_add_u64 v[0:1], v[38:39], 0, v[0:1]
	v_mov_b32_e32 v38, v35
	v_cvt_pk_fp8_f32 v38, v22, v23
	s_waitcnt lgkmcnt(1)
	v_mfma_f32_16x16x32_f16 v[18:21], v[18:21], v[30:33], 0
	v_mov_b32_e32 v39, v35
	v_cvt_pk_fp8_f32 v39, v26, v27
	v_cvt_pk_fp8_f32 v38, v24, v25 op_sel:[0,0,1]
	v_mfma_f32_16x16x32_f16 v[10:13], v[50:53], v[2:5], v[10:13]
	ds_read_b128 v[22:25], v37 offset:30592
	ds_read_b128 v[50:53], v37 offset:30656
	global_store_dwordx2 v[0:1], v[62:63], off
	v_cvt_pk_fp8_f32 v39, v28, v29 op_sel:[0,0,1]
	s_waitcnt lgkmcnt(2)
	v_mfma_f32_16x16x32_f16 v[18:21], v[54:57], v[14:17], v[18:21]
	ds_read_b128 v[26:29], v37 offset:34816
	ds_read_b128 v[54:57], v37 offset:34880
	v_cvt_pk_fp8_f32 v58, v44, v45 op_sel:[0,0,1]
	v_permlane16_swap_b32_e32 v38, v39
	s_waitcnt lgkmcnt(3)
	v_mfma_f32_16x16x32_f16 v[18:21], v[22:25], v[6:9], v[18:21]
	ds_read_b128 v[22:25], v37 offset:34944
	ds_read_b128 v[42:45], v37 offset:35008
	global_store_dwordx2 v[0:1], v[38:39], off offset:32
	v_mov_b32_e32 v38, v35
	s_waitcnt lgkmcnt(4)
	v_mfma_f32_16x16x32_f16 v[18:21], v[50:53], v[2:5], v[18:21]
	v_mov_b32_e32 v39, v35
	v_cvt_pk_fp8_f32 v59, v46, v47
	v_cvt_pk_fp8_f32 v38, v10, v11
	s_waitcnt lgkmcnt(3)
	v_mfma_f32_16x16x32_f16 v[26:29], v[26:29], v[30:33], 0
	v_cvt_pk_fp8_f32 v59, v48, v49 op_sel:[0,0,1]
	s_nop 1
	v_cvt_pk_fp8_f32 v39, v18, v19
	s_waitcnt lgkmcnt(2)
	v_mfma_f32_16x16x32_f16 v[14:17], v[54:57], v[14:17], v[26:29]
	v_cvt_pk_fp8_f32 v38, v12, v13 op_sel:[0,0,1]
	v_permlane16_swap_b32_e32 v58, v59
	v_cvt_pk_fp8_f32 v39, v20, v21 op_sel:[0,0,1]
	s_waitcnt lgkmcnt(1)
	v_mfma_f32_16x16x32_f16 v[6:9], v[22:25], v[6:9], v[14:17]
	global_store_dwordx2 v[0:1], v[58:59], off offset:64
	v_permlane16_swap_b32_e32 v38, v39
	global_store_dwordx2 v[0:1], v[38:39], off offset:96
	s_waitcnt lgkmcnt(0)
	v_mfma_f32_16x16x32_f16 v[0:3], v[42:45], v[2:5], v[6:9]
	s_and_saveexec_b64 s[2:3], vcc
	s_xor_b64 s[2:3], exec, s[2:3]
	s_cbranch_execz .LBB1_77
	v_lshlrev_b64 v[4:5], 5, v[34:35]
	v_lshlrev_b32_e32 v34, 4, v40
	s_waitcnt lgkmcnt(0)
	v_lshl_add_u64 v[4:5], s[26:27], 0, v[4:5]
	v_lshl_add_u64 v[4:5], v[4:5], 0, v[34:35]
	global_store_dwordx4 v[4:5], v[0:3], off offset:-32
.LBB1_77:
	s_andn2_saveexec_b64 s[2:3], s[2:3]
	s_cbranch_execz .LBB1_79
	s_nop 1
	v_cvt_pk_f16_f32 v3, v2, v3
	v_cvt_pk_f16_f32 v2, v0, v1
	v_mov_b32_e32 v37, 0
	s_waitcnt lgkmcnt(0)
	v_lshl_add_u64 v[0:1], v[34:35], 4, s[24:25]
	v_lshl_add_u64 v[0:1], v[0:1], 0, v[36:37]
	global_store_dwordx2 v[0:1], v[2:3], off

	.amdhsa_kernel _Z13second_kernelPKfPKDF16_PDF16_PfS4_PKjPKiPiS9_
		.amdhsa_group_segment_fixed_size 40960
		.amdhsa_private_segment_fixed_size 0
		.amdhsa_kernarg_size 72
		.amdhsa_user_sgpr_count 2
		.amdhsa_user_sgpr_dispatch_ptr 0
		.amdhsa_user_sgpr_queue_ptr 0
		.amdhsa_user_sgpr_kernarg_segment_ptr 1
		.amdhsa_user_sgpr_dispatch_id 0
		.amdhsa_user_sgpr_kernarg_preload_length 0
		.amdhsa_user_sgpr_kernarg_preload_offset 0
		.amdhsa_user_sgpr_private_segment_size 0
		.amdhsa_uses_dynamic_stack 0
		.amdhsa_enable_private_segment 0
		.amdhsa_system_sgpr_workgroup_id_x 1
		.amdhsa_system_sgpr_workgroup_id_y 0
		.amdhsa_system_sgpr_workgroup_id_z 0
		.amdhsa_system_sgpr_workgroup_info 0
		.amdhsa_system_vgpr_workitem_id 0
		.amdhsa_next_free_vgpr 64
		.amdhsa_next_free_sgpr 28
		.amdhsa_accum_offset 64
		.amdhsa_reserve_vcc 1
		.amdhsa_float_round_mode_32 0
		.amdhsa_float_round_mode_16_64 0
		.amdhsa_float_denorm_mode_32 3
		.amdhsa_float_denorm_mode_16_64 3
		.amdhsa_dx10_clamp 1
		.amdhsa_ieee_mode 1
		.amdhsa_fp16_overflow 0
		.amdhsa_tg_split 0
		.amdhsa_exception_fp_ieee_invalid_op 0
		.amdhsa_exception_fp_denorm_src 0
		.amdhsa_exception_fp_ieee_div_zero 0
		.amdhsa_exception_fp_ieee_overflow 0
		.amdhsa_exception_fp_ieee_underflow 0
		.amdhsa_exception_fp_ieee_inexact 0
		.amdhsa_exception_int_div_zero 0
	.end_amdhsa_kernel

_Z11agg1_kernelPKDF16_PKfS2_PKiS4_S2_S2_PDF16_PfS6_i:
	s_load_dwordx8 s[4:11], s[0:1], 0x0
	s_load_dwordx8 s[12:19], s[0:1], 0x20
	s_load_dwordx4 s[20:23], s[0:1], 0x40
	s_load_dword s24, s[0:1], 0x50
	v_lshlrev_b32_e32 v32, 2, v0
	v_readfirstlane_b32 s25, v0
	s_lshl_b32 s26, s2, 5
	v_and_b32_e32 v64, 7, v0
	v_bfe_u32 v65, v0, 3, 3
	v_and_b32_e32 v45, 31, v0
	s_lshr_b32 s25, s25, 6
	v_lshlrev_b32_e32 v1, 1, v64
	v_add_u32_e32 v46, s26, v45
	s_waitcnt lgkmcnt(0)
	global_load_dword v33, v32, s[14:15]
	global_load_dword v34, v32, s[16:17]
	s_add_i32 s28, s24, -1
	v_cmp_gt_i32_e64 s[38:39], s24, v46
	v_min_i32_e32 v46, s28, v46
	v_lshlrev_b32_e32 v47, 2, v46
	global_load_dword v44, v47, s[10:11]
	global_load_dword v48, v47, s[10:11] offset:4
	s_lshl_b32 s27, s25, 11
	v_lshlrev_b32_e32 v62, 6, v64
	v_add_u32_e32 v62, 0x2000, v62
	v_cmp_eq_u32_e64 s[34:35], 0, v64
	v_lshlrev_b32_e32 v35, 8, v64
	v_lshl_add_u32 v35, v65, 4, v35
	v_add_u32_e32 v63, s27, v35
	v_mov_b32_e32 v36, 0
	v_mov_b32_e32 v37, 0
	v_mov_b32_e32 v38, 0
	v_mov_b32_e32 v39, 0
	s_waitcnt vmcnt(2)
	ds_write2st64_b32 v32, v33, v34 offset0:32 offset1:36
	ds_write_b128 v63, v[36:39]
	ds_write_b128 v63, v[36:39] offset:128
	s_waitcnt vmcnt(0)
	v_sub_u32_e32 v48, v48, v44
	v_add_u32_e32 v48, 1, v48
	v_cndmask_b32_e64 v48, 0, v48, s[38:39]
	v_lshl_or_b32 v40, v48, 5, v45
	s_nop 1
	v_mov_b32_dpp v41, v40 quad_perm:[1,0,3,2] row_mask:0xf bank_mask:0xf
	s_mov_b32 s40, 0x99999999
	s_mov_b32 s41, 0x99999999
	v_min_u32_e32 v42, v40, v41
	v_max_u32_e32 v43, v40, v41
	v_cndmask_b32_e64 v40, v42, v43, s[40:41]
	s_nop 1
	v_mov_b32_dpp v41, v40 quad_perm:[2,3,0,1] row_mask:0xf bank_mask:0xf
	s_mov_b32 s40, 0xc3c3c3c3
	s_mov_b32 s41, 0xc3c3c3c3
	v_min_u32_e32 v42, v40, v41
	v_max_u32_e32 v43, v40, v41
	v_cndmask_b32_e64 v40, v42, v43, s[40:41]
	s_nop 1
	v_mov_b32_dpp v41, v40 quad_perm:[1,0,3,2] row_mask:0xf bank_mask:0xf
	s_mov_b32 s40, 0xa5a5a5a5
	s_mov_b32 s41, 0xa5a5a5a5
	v_min_u32_e32 v42, v40, v41
	v_max_u32_e32 v43, v40, v41
	v_cndmask_b32_e64 v40, v42, v43, s[40:41]
	s_nop 1
	v_mov_b32_dpp v41, v40 row_shl:4 row_mask:0xf bank_mask:0x5
	v_mov_b32_dpp v41, v40 row_shr:4 row_mask:0xf bank_mask:0xa
	s_mov_b32 s40, 0xf00ff00f
	s_mov_b32 s41, 0xf00ff00f
	v_min_u32_e32 v42, v40, v41
	v_max_u32_e32 v43, v40, v41
	v_cndmask_b32_e64 v40, v42, v43, s[40:41]
	s_nop 1
	v_mov_b32_dpp v41, v40 quad_perm:[2,3,0,1] row_mask:0xf bank_mask:0xf
	s_mov_b32 s40, 0xcc33cc33
	s_mov_b32 s41, 0xcc33cc33
	v_min_u32_e32 v42, v40, v41
	v_max_u32_e32 v43, v40, v41
	v_cndmask_b32_e64 v40, v42, v43, s[40:41]
	s_nop 1
	v_mov_b32_dpp v41, v40 quad_perm:[1,0,3,2] row_mask:0xf bank_mask:0xf
	s_mov_b32 s40, 0xaa55aa55
	s_mov_b32 s41, 0xaa55aa55
	v_min_u32_e32 v42, v40, v41
	v_max_u32_e32 v43, v40, v41
	v_cndmask_b32_e64 v40, v42, v43, s[40:41]
	s_nop 1
	v_mov_b32_dpp v41, v40 row_ror:8 row_mask:0xf bank_mask:0xf
	s_mov_b32 s40, 0xff0000ff
	s_mov_b32 s41, 0xff0000ff
	v_min_u32_e32 v42, v40, v41
	v_max_u32_e32 v43, v40, v41
	v_cndmask_b32_e64 v40, v42, v43, s[40:41]
	s_nop 1
	v_mov_b32_dpp v41, v40 row_shl:4 row_mask:0xf bank_mask:0x5
	v_mov_b32_dpp v41, v40 row_shr:4 row_mask:0xf bank_mask:0xa
	s_mov_b32 s40, 0xf0f00f0f
	s_mov_b32 s41, 0xf0f00f0f
	v_min_u32_e32 v42, v40, v41
	v_max_u32_e32 v43, v40, v41
	v_cndmask_b32_e64 v40, v42, v43, s[40:41]
	s_nop 1
	v_mov_b32_dpp v41, v40 quad_perm:[2,3,0,1] row_mask:0xf bank_mask:0xf
	s_mov_b32 s40, 0xcccc3333
	s_mov_b32 s41, 0xcccc3333
	v_min_u32_e32 v42, v40, v41
	v_max_u32_e32 v43, v40, v41
	v_cndmask_b32_e64 v40, v42, v43, s[40:41]
	s_nop 1
	v_mov_b32_dpp v41, v40 quad_perm:[1,0,3,2] row_mask:0xf bank_mask:0xf
	s_mov_b32 s40, 0xaaaa5555
	s_mov_b32 s41, 0xaaaa5555
	v_min_u32_e32 v42, v40, v41
	v_max_u32_e32 v43, v40, v41
	v_cndmask_b32_e64 v40, v42, v43, s[40:41]
	ds_swizzle_b32 v41, v40 offset:swizzle(SWAP,16)
	s_waitcnt lgkmcnt(0)
	s_mov_b32 s40, 0xffff
	s_mov_b32 s41, 0xffff
	v_min_u32_e32 v42, v40, v41
	v_max_u32_e32 v43, v40, v41
	v_cndmask_b32_e64 v40, v42, v43, s[40:41]
	s_nop 1
	v_mov_b32_dpp v41, v40 row_ror:8 row_mask:0xf bank_mask:0xf
	s_mov_b32 s40, 0xff00ff
	s_mov_b32 s41, 0xff00ff
	v_min_u32_e32 v42, v40, v41
	v_max_u32_e32 v43, v40, v41
	v_cndmask_b32_e64 v40, v42, v43, s[40:41]
	s_nop 1
	v_mov_b32_dpp v41, v40 row_shl:4 row_mask:0xf bank_mask:0x5
	v_mov_b32_dpp v41, v40 row_shr:4 row_mask:0xf bank_mask:0xa
	s_mov_b32 s40, 0xf0f0f0f
	s_mov_b32 s41, 0xf0f0f0f
	v_min_u32_e32 v42, v40, v41
	v_max_u32_e32 v43, v40, v41
	v_cndmask_b32_e64 v40, v42, v43, s[40:41]
	s_nop 1
	v_mov_b32_dpp v41, v40 quad_perm:[2,3,0,1] row_mask:0xf bank_mask:0xf
	s_mov_b32 s40, 0x33333333
	s_mov_b32 s41, 0x33333333
	v_min_u32_e32 v42, v40, v41
	v_max_u32_e32 v43, v40, v41
	v_cndmask_b32_e64 v40, v42, v43, s[40:41]
	s_nop 1
	v_mov_b32_dpp v41, v40 quad_perm:[1,0,3,2] row_mask:0xf bank_mask:0xf
	s_mov_b32 s40, 0x55555555
	s_mov_b32 s41, 0x55555555
	v_min_u32_e32 v42, v40, v41
	v_max_u32_e32 v43, v40, v41
	v_cndmask_b32_e64 v40, v42, v43, s[40:41]
	s_lshl_b32 s40, s25, 3
	v_add_u32_e32 v45, s40, v65
	v_lshlrev_b32_e32 v45, 2, v45
	ds_bpermute_b32 v46, v45, v40
	s_waitcnt lgkmcnt(0)
	v_and_b32_e32 v15, 31, v46
	v_lshrrev_b32_e32 v11, 5, v46
	v_lshlrev_b32_e32 v47, 2, v15
	ds_bpermute_b32 v10, v47, v44
	v_add_u32_e32 v66, s26, v15
	v_min_i32_e32 v66, s28, v66
	v_cmp_lt_u32_e64 s[36:37], 0, v11
	v_lshlrev_b32_e32 v4, 2, v66
	v_lshlrev_b32_e32 v35, 2, v64
	v_lshl_or_b32 v35, v66, 5, v35
	global_load_dword v9, v35, s[8:9]
	v_lshrrev_b32_e32 v3, 3, v15
	v_lshlrev_b32_e32 v3, 11, v3
	v_and_b32_e32 v47, 7, v15
	v_lshl_add_u32 v3, v47, 1, v3
	v_lshl_add_u32 v3, v64, 4, v3
	v_readfirstlane_b32 s29, v11
	s_waitcnt lgkmcnt(0)
	s_barrier
	v_add_u32_e32 v67, v10, v64
	v_lshlrev_b32_e32 v67, 2, v67
	v_mov_b32_e32 v5, s24
	v_mov_b32_e32 v6, s24
	v_mov_b32_e32 v7, s24
	v_mov_b32_e32 v8, s24
	v_mov_b32_e32 v69, s24
	v_cndmask_b32_e64 v5, v5, v66, s[34:35]
	v_cmp_gt_i32_e32 vcc, v11, v64
	s_andn2_b64 s[40:41], vcc, s[34:35]
	s_and_saveexec_b64 s[32:33], s[40:41]
	global_load_dword v5, v67, s[12:13] offset:-4
	s_mov_b64 exec, s[32:33]
	v_add_u32_e32 v68, 8, v64
	v_cmp_gt_i32_e32 vcc, v11, v68
	s_and_saveexec_b64 s[32:33], vcc
	global_load_dword v6, v67, s[12:13] offset:28
	s_mov_b64 exec, s[32:33]
	v_add_u32_e32 v68, 16, v64
	v_cmp_gt_i32_e32 vcc, v11, v68
	s_and_saveexec_b64 s[32:33], vcc
	global_load_dword v7, v67, s[12:13] offset:60
	s_mov_b64 exec, s[32:33]
	v_add_u32_e32 v68, 24, v64
	v_cmp_gt_i32_e32 vcc, v11, v68
	s_and_saveexec_b64 s[32:33], vcc
	global_load_dword v8, v67, s[12:13] offset:92
	s_mov_b64 exec, s[32:33]
	v_add_u32_e32 v68, 32, v64
	v_cmp_gt_i32_e32 vcc, v11, v68
	s_and_saveexec_b64 s[32:33], vcc
	global_load_dword v69, v67, s[12:13] offset:124
	s_mov_b64 exec, s[32:33]
	s_waitcnt vmcnt(0)
	v_lshlrev_b32_e32 v5, 4, v5
	v_lshlrev_b32_e32 v6, 4, v6
	v_lshlrev_b32_e32 v7, 4, v7
	v_lshlrev_b32_e32 v8, 4, v8
	v_lshlrev_b32_e32 v69, 4, v69
	s_mov_b32 s42, 0
	s_mov_b32 s43, 0
	ds_swizzle_b32 v32, v5 offset:swizzle(BITMASK_PERM, "pp000")
	ds_swizzle_b32 v33, v5 offset:swizzle(BITMASK_PERM, "pp001")
	ds_swizzle_b32 v34, v5 offset:swizzle(BITMASK_PERM, "pp010")
	ds_swizzle_b32 v35, v5 offset:swizzle(BITMASK_PERM, "pp011")
	s_cmp_lt_i32 s29, 3
	s_cbranch_scc1 .Lagg_first_half
	s_waitcnt lgkmcnt(0)
	v_or_b32_e32 v32, v32, v1
	v_or_b32_e32 v33, v33, v1
	v_or_b32_e32 v34, v34, v1
	v_or_b32_e32 v35, v35, v1
	global_load_ushort v36, v32, s[6:7]
	global_load_ushort v37, v33, s[6:7]
	global_load_ushort v38, v34, s[6:7]
	global_load_ushort v39, v35, s[6:7]
	v_lshlrev_b32_e32 v32, 3, v32
	v_lshlrev_b32_e32 v33, 3, v33
	v_lshlrev_b32_e32 v34, 3, v34
	v_lshlrev_b32_e32 v35, 3, v35
	global_load_dwordx4 v[40:43], v32, s[4:5]
	global_load_dwordx4 v[44:47], v33, s[4:5]
	global_load_dwordx4 v[48:51], v34, s[4:5]
	global_load_dwordx4 v[52:55], v35, s[4:5]
	ds_swizzle_b32 v32, v5 offset:swizzle(BITMASK_PERM, "pp100")
	ds_swizzle_b32 v33, v5 offset:swizzle(BITMASK_PERM, "pp101")
	ds_swizzle_b32 v34, v5 offset:swizzle(BITMASK_PERM, "pp110")
	ds_swizzle_b32 v35, v5 offset:swizzle(BITMASK_PERM, "pp111")
	s_waitcnt vmcnt(4)
	v_fma_mix_f32 v36, v36, 1.0, v9 op_sel_hi:[1,0,0]
	v_fma_mix_f32 v37, v37, 1.0, v9 op_sel_hi:[1,0,0]
	v_fma_mix_f32 v38, v38, 1.0, v9 op_sel_hi:[1,0,0]
	v_fma_mix_f32 v39, v39, 1.0, v9 op_sel_hi:[1,0,0]
	v_mul_f32_e32 v58, 0x3e4ccccd, v36
	v_mul_f32_e32 v59, 0x3e4ccccd, v37
	v_mul_f32_e32 v60, 0x3e4ccccd, v38
	v_mul_f32_e32 v61, 0x3e4ccccd, v39
	v_max_f32_e32 v36, v36, v58
	v_max_f32_e32 v37, v37, v59
	v_max_f32_e32 v38, v38, v60
	v_max_f32_e32 v39, v39, v61
	v_max3_f32 v56, v36, v37, v38
	v_max_f32_e32 v13, v56, v39
	v_sub_f32_e32 v36, v36, v13
	v_sub_f32_e32 v37, v37, v13
	v_sub_f32_e32 v38, v38, v13
	v_sub_f32_e32 v39, v39, v13
	v_exp_f32_e32 v36, v36
	v_exp_f32_e32 v37, v37
	v_exp_f32_e32 v38, v38
	v_exp_f32_e32 v39, v39
	s_nop 0
	v_add_f32_e32 v14, v36, v37
	v_add_f32_e32 v14, v14, v38
	v_add_f32_e32 v14, v14, v39
	s_waitcnt vmcnt(3)
	v_cvt_scalef32_pk_f16_fp8 v58, v40, 1.0
	v_cvt_scalef32_pk_f16_fp8 v59, v40, 1.0 op_sel:[1,0,0]
	v_cvt_scalef32_pk_f16_fp8 v60, v41, 1.0
	v_cvt_scalef32_pk_f16_fp8 v61, v41, 1.0 op_sel:[1,0,0]
	v_fma_mix_f32 v16, v58, v36, 0 op_sel_hi:[1,0,0]
	v_fma_mix_f32 v17, v58, v36, 0 op_sel:[1,0,0] op_sel_hi:[1,0,0]
	v_fma_mix_f32 v18, v59, v36, 0 op_sel_hi:[1,0,0]
	v_fma_mix_f32 v19, v59, v36, 0 op_sel:[1,0,0] op_sel_hi:[1,0,0]
	v_fma_mix_f32 v20, v60, v36, 0 op_sel_hi:[1,0,0]
	v_fma_mix_f32 v21, v60, v36, 0 op_sel:[1,0,0] op_sel_hi:[1,0,0]
	v_fma_mix_f32 v22, v61, v36, 0 op_sel_hi:[1,0,0]
	v_fma_mix_f32 v23, v61, v36, 0 op_sel:[1,0,0] op_sel_hi:[1,0,0]
	v_cvt_scalef32_pk_f16_fp8 v58, v42, 1.0
	v_cvt_scalef32_pk_f16_fp8 v59, v42, 1.0 op_sel:[1,0,0]
	v_cvt_scalef32_pk_f16_fp8 v60, v43, 1.0
	v_cvt_scalef32_pk_f16_fp8 v61, v43, 1.0 op_sel:[1,0,0]
	v_fma_mix_f32 v24, v58, v36, 0 op_sel_hi:[1,0,0]
	v_fma_mix_f32 v25, v58, v36, 0 op_sel:[1,0,0] op_sel_hi:[1,0,0]
	v_fma_mix_f32 v26, v59, v36, 0 op_sel_hi:[1,0,0]
	v_fma_mix_f32 v27, v59, v36, 0 op_sel:[1,0,0] op_sel_hi:[1,0,0]
	v_fma_mix_f32 v28, v60, v36, 0 op_sel_hi:[1,0,0]
	v_fma_mix_f32 v29, v60, v36, 0 op_sel:[1,0,0] op_sel_hi:[1,0,0]
	v_fma_mix_f32 v30, v61, v36, 0 op_sel_hi:[1,0,0]
	v_fma_mix_f32 v31, v61, v36, 0 op_sel:[1,0,0] op_sel_hi:[1,0,0]
	s_waitcnt vmcnt(2)
	v_cvt_scalef32_pk_f16_fp8 v58, v44, 1.0
	v_cvt_scalef32_pk_f16_fp8 v59, v44, 1.0 op_sel:[1,0,0]
	v_cvt_scalef32_pk_f16_fp8 v60, v45, 1.0
	v_cvt_scalef32_pk_f16_fp8 v61, v45, 1.0 op_sel:[1,0,0]
	v_fma_mix_f32 v16, v58, v37, v16 op_sel_hi:[1,0,0]
	v_fma_mix_f32 v17, v58, v37, v17 op_sel:[1,0,0] op_sel_hi:[1,0,0]
	v_fma_mix_f32 v18, v59, v37, v18 op_sel_hi:[1,0,0]
	v_fma_mix_f32 v19, v59, v37, v19 op_sel:[1,0,0] op_sel_hi:[1,0,0]
	v_fma_mix_f32 v20, v60, v37, v20 op_sel_hi:[1,0,0]
	v_fma_mix_f32 v21, v60, v37, v21 op_sel:[1,0,0] op_sel_hi:[1,0,0]
	v_fma_mix_f32 v22, v61, v37, v22 op_sel_hi:[1,0,0]
	v_fma_mix_f32 v23, v61, v37, v23 op_sel:[1,0,0] op_sel_hi:[1,0,0]
	v_cvt_scalef32_pk_f16_fp8 v58, v46, 1.0
	v_cvt_scalef32_pk_f16_fp8 v59, v46, 1.0 op_sel:[1,0,0]
	v_cvt_scalef32_pk_f16_fp8 v60, v47, 1.0
	v_cvt_scalef32_pk_f16_fp8 v61, v47, 1.0 op_sel:[1,0,0]
	v_fma_mix_f32 v24, v58, v37, v24 op_sel_hi:[1,0,0]
	v_fma_mix_f32 v25, v58, v37, v25 op_sel:[1,0,0] op_sel_hi:[1,0,0]
	v_fma_mix_f32 v26, v59, v37, v26 op_sel_hi:[1,0,0]
	v_fma_mix_f32 v27, v59, v37, v27 op_sel:[1,0,0] op_sel_hi:[1,0,0]
	v_fma_mix_f32 v28, v60, v37, v28 op_sel_hi:[1,0,0]
	v_fma_mix_f32 v29, v60, v37, v29 op_sel:[1,0,0] op_sel_hi:[1,0,0]
	v_fma_mix_f32 v30, v61, v37, v30 op_sel_hi:[1,0,0]
	v_fma_mix_f32 v31, v61, v37, v31 op_sel:[1,0,0] op_sel_hi:[1,0,0]
	s_waitcnt vmcnt(1)
	v_cvt_scalef32_pk_f16_fp8 v58, v48, 1.0
	v_cvt_scalef32_pk_f16_fp8 v59, v48, 1.0 op_sel:[1,0,0]
	v_cvt_scalef32_pk_f16_fp8 v60, v49, 1.0
	v_cvt_scalef32_pk_f16_fp8 v61, v49, 1.0 op_sel:[1,0,0]
	v_fma_mix_f32 v16, v58, v38, v16 op_sel_hi:[1,0,0]
	v_fma_mix_f32 v17, v58, v38, v17 op_sel:[1,0,0] op_sel_hi:[1,0,0]
	v_fma_mix_f32 v18, v59, v38, v18 op_sel_hi:[1,0,0]
	v_fma_mix_f32 v19, v59, v38, v19 op_sel:[1,0,0] op_sel_hi:[1,0,0]
	v_fma_mix_f32 v20, v60, v38, v20 op_sel_hi:[1,0,0]
	v_fma_mix_f32 v21, v60, v38, v21 op_sel:[1,0,0] op_sel_hi:[1,0,0]
	v_fma_mix_f32 v22, v61, v38, v22 op_sel_hi:[1,0,0]
	v_fma_mix_f32 v23, v61, v38, v23 op_sel:[1,0,0] op_sel_hi:[1,0,0]
	v_cvt_scalef32_pk_f16_fp8 v58, v50, 1.0
	v_cvt_scalef32_pk_f16_fp8 v59, v50, 1.0 op_sel:[1,0,0]
	v_cvt_scalef32_pk_f16_fp8 v60, v51, 1.0
	v_cvt_scalef32_pk_f16_fp8 v61, v51, 1.0 op_sel:[1,0,0]
	v_fma_mix_f32 v24, v58, v38, v24 op_sel_hi:[1,0,0]
	v_fma_mix_f32 v25, v58, v38, v25 op_sel:[1,0,0] op_sel_hi:[1,0,0]
	v_fma_mix_f32 v26, v59, v38, v26 op_sel_hi:[1,0,0]
	v_fma_mix_f32 v27, v59, v38, v27 op_sel:[1,0,0] op_sel_hi:[1,0,0]
	v_fma_mix_f32 v28, v60, v38, v28 op_sel_hi:[1,0,0]
	v_fma_mix_f32 v29, v60, v38, v29 op_sel:[1,0,0] op_sel_hi:[1,0,0]
	v_fma_mix_f32 v30, v61, v38, v30 op_sel_hi:[1,0,0]
	v_fma_mix_f32 v31, v61, v38, v31 op_sel:[1,0,0] op_sel_hi:[1,0,0]
	s_waitcnt vmcnt(0)
	v_cvt_scalef32_pk_f16_fp8 v58, v52, 1.0
	v_cvt_scalef32_pk_f16_fp8 v59, v52, 1.0 op_sel:[1,0,0]
	v_cvt_scalef32_pk_f16_fp8 v60, v53, 1.0
	v_cvt_scalef32_pk_f16_fp8 v61, v53, 1.0 op_sel:[1,0,0]
	v_fma_mix_f32 v16, v58, v39, v16 op_sel_hi:[1,0,0]
	v_fma_mix_f32 v17, v58, v39, v17 op_sel:[1,0,0] op_sel_hi:[1,0,0]
	v_fma_mix_f32 v18, v59, v39, v18 op_sel_hi:[1,0,0]
	v_fma_mix_f32 v19, v59, v39, v19 op_sel:[1,0,0] op_sel_hi:[1,0,0]
	v_fma_mix_f32 v20, v60, v39, v20 op_sel_hi:[1,0,0]
	v_fma_mix_f32 v21, v60, v39, v21 op_sel:[1,0,0] op_sel_hi:[1,0,0]
	v_fma_mix_f32 v22, v61, v39, v22 op_sel_hi:[1,0,0]
	v_fma_mix_f32 v23, v61, v39, v23 op_sel:[1,0,0] op_sel_hi:[1,0,0]
	v_cvt_scalef32_pk_f16_fp8 v58, v54, 1.0
	v_cvt_scalef32_pk_f16_fp8 v59, v54, 1.0 op_sel:[1,0,0]
	v_cvt_scalef32_pk_f16_fp8 v60, v55, 1.0
	v_cvt_scalef32_pk_f16_fp8 v61, v55, 1.0 op_sel:[1,0,0]
	v_fma_mix_f32 v24, v58, v39, v24 op_sel_hi:[1,0,0]
	v_fma_mix_f32 v25, v58, v39, v25 op_sel:[1,0,0] op_sel_hi:[1,0,0]
	v_fma_mix_f32 v26, v59, v39, v26 op_sel_hi:[1,0,0]
	v_fma_mix_f32 v27, v59, v39, v27 op_sel:[1,0,0] op_sel_hi:[1,0,0]
	v_fma_mix_f32 v28, v60, v39, v28 op_sel_hi:[1,0,0]
	v_fma_mix_f32 v29, v60, v39, v29 op_sel:[1,0,0] op_sel_hi:[1,0,0]
	v_fma_mix_f32 v30, v61, v39, v30 op_sel_hi:[1,0,0]
	v_fma_mix_f32 v31, v61, v39, v31 op_sel:[1,0,0] op_sel_hi:[1,0,0]
	s_sub_i32 s29, s29, 4
	s_branch .Lagg_B

amdhsa.kernels:
  - .agpr_count:     0
    .args:
      - .actual_access:  read_only
        .address_space:  global
        .offset:         0
        .size:           8
        .value_kind:     global_buffer
      - .actual_access:  read_only
        .address_space:  global
        .offset:         8
        .size:           8
        .value_kind:     global_buffer
      - .actual_access:  read_only
        .address_space:  global
        .offset:         16
        .size:           8
        .value_kind:     global_buffer
      - .actual_access:  read_only
        .address_space:  global
        .offset:         24
        .size:           8
        .value_kind:     global_buffer
      - .actual_access:  read_only
        .address_space:  global
        .offset:         32
        .size:           8
        .value_kind:     global_buffer
      - .actual_access:  read_only
        .address_space:  global
        .offset:         40
        .size:           8
        .value_kind:     global_buffer
      - .actual_access:  read_only
        .address_space:  global
        .offset:         48
        .size:           8
        .value_kind:     global_buffer
      - .actual_access:  read_only
        .address_space:  global
        .offset:         56
        .size:           8
        .value_kind:     global_buffer
      - .actual_access:  read_only
        .address_space:  global
        .offset:         64
        .size:           8
        .value_kind:     global_buffer
      - .actual_access:  read_only
        .address_space:  global
        .offset:         72
        .size:           8
        .value_kind:     global_buffer
      - .actual_access:  read_only
        .address_space:  global
        .offset:         80
        .size:           8
        .value_kind:     global_buffer
      - .actual_access:  read_only
        .address_space:  global
        .offset:         88
        .size:           8
        .value_kind:     global_buffer
      - .actual_access:  read_only
        .address_space:  global
        .offset:         96
        .size:           8
        .value_kind:     global_buffer
      - .actual_access:  write_only
        .address_space:  global
        .offset:         104
        .size:           8
        .value_kind:     global_buffer
      - .actual_access:  write_only
        .address_space:  global
        .offset:         112
        .size:           8
        .value_kind:     global_buffer
      - .actual_access:  write_only
        .address_space:  global
        .offset:         120
        .size:           8
        .value_kind:     global_buffer
      - .actual_access:  write_only
        .address_space:  global
        .offset:         128
        .size:           8
        .value_kind:     global_buffer
      - .actual_access:  write_only
        .address_space:  global
        .offset:         136
        .size:           8
        .value_kind:     global_buffer
      - .actual_access:  write_only
        .address_space:  global
        .offset:         144
        .size:           8
        .value_kind:     global_buffer
      - .actual_access:  write_only
        .address_space:  global
        .offset:         152
        .size:           8
        .value_kind:     global_buffer
      - .actual_access:  write_only
        .address_space:  global
        .offset:         160
        .size:           8
        .value_kind:     global_buffer
      - .actual_access:  write_only
        .address_space:  global
        .offset:         168
        .size:           8
        .value_kind:     global_buffer
      - .actual_access:  read_only
        .address_space:  global
        .offset:         176
        .size:           8
        .value_kind:     global_buffer
    .group_segment_fixed_size: 29696
    .kernarg_segment_align: 8
    .kernarg_segment_size: 184
    .language:       OpenCL C
    .language_version:
      - 2
      - 0
    .max_flat_workgroup_size: 512
    .name:           _Z12front_kernelPKiS0_PKfS2_S2_S2_S2_S2_S2_S2_S2_S2_S2_PjS3_PiS4_PDF16_PfS6_S4_S5_S0_
    .private_segment_fixed_size: 0
    .sgpr_count:     30
    .sgpr_spill_count: 0
    .symbol:         _Z12front_kernelPKiS0_PKfS2_S2_S2_S2_S2_S2_S2_S2_S2_S2_PjS3_PiS4_PDF16_PfS6_S4_S5_S0_.kd
    .uniform_work_group_size: 1
    .uses_dynamic_stack: false
    .vgpr_count:     80
    .vgpr_spill_count: 0
    .wavefront_size: 64
  - .agpr_count:     0
    .args:
      - .actual_access:  read_only
        .address_space:  global
        .offset:         0
        .size:           8
        .value_kind:     global_buffer
      - .actual_access:  read_only
        .address_space:  global
        .offset:         8
        .size:           8
        .value_kind:     global_buffer
      - .actual_access:  write_only
        .address_space:  global
        .offset:         16
        .size:           8
        .value_kind:     global_buffer
      - .actual_access:  write_only
        .address_space:  global
        .offset:         24
        .size:           8
        .value_kind:     global_buffer
      - .actual_access:  write_only
        .address_space:  global
        .offset:         32
        .size:           8
        .value_kind:     global_buffer
      - .actual_access:  read_only
        .address_space:  global
        .offset:         40
        .size:           8
        .value_kind:     global_buffer
      - .actual_access:  read_only
        .address_space:  global
        .offset:         48
        .size:           8
        .value_kind:     global_buffer
      - .actual_access:  write_only
        .address_space:  global
        .offset:         56
        .size:           8
        .value_kind:     global_buffer
      - .actual_access:  write_only
        .address_space:  global
        .offset:         64
        .size:           8
        .value_kind:     global_buffer
    .group_segment_fixed_size: 40960
    .kernarg_segment_align: 8
    .kernarg_segment_size: 72
    .language:       OpenCL C
    .language_version:
      - 2
      - 0
    .max_flat_workgroup_size: 512
    .name:           _Z13second_kernelPKfPKDF16_PDF16_PfS4_PKjPKiPiS9_
    .private_segment_fixed_size: 0
    .sgpr_count:     34
    .sgpr_spill_count: 0
    .symbol:         _Z13second_kernelPKfPKDF16_PDF16_PfS4_PKjPKiPiS9_.kd
    .uniform_work_group_size: 1
    .uses_dynamic_stack: false
    .vgpr_count:     64
    .vgpr_spill_count: 0
    .wavefront_size: 64
  - .agpr_count:     0
    .args:
      - .actual_access:  read_only
        .address_space:  global
        .offset:         0
        .size:           8
        .value_kind:     global_buffer
      - .actual_access:  read_only
        .address_space:  global
        .offset:         8
        .size:           8
        .value_kind:     global_buffer
      - .actual_access:  read_only
        .address_space:  global
        .offset:         16
        .size:           8
        .value_kind:     global_buffer
      - .actual_access:  read_only
        .address_space:  global
        .offset:         24
        .size:           8
        .value_kind:     global_buffer
      - .actual_access:  read_only
        .address_space:  global
        .offset:         32
        .size:           8
        .value_kind:     global_buffer
      - .actual_access:  read_only
        .address_space:  global
        .offset:         40
        .size:           8
        .value_kind:     global_buffer
      - .actual_access:  read_only
        .address_space:  global
        .offset:         48
        .size:           8
        .value_kind:     global_buffer
      - .actual_access:  write_only
        .address_space:  global
        .offset:         56
        .size:           8
        .value_kind:     global_buffer
      - .actual_access:  write_only
        .address_space:  global
        .offset:         64
        .size:           8
        .value_kind:     global_buffer
      - .actual_access:  write_only
        .address_space:  global
        .offset:         72
        .size:           8
        .value_kind:     global_buffer
      - .offset:         80
        .size:           4
        .value_kind:     by_value
    .group_segment_fixed_size: 10240
    .kernarg_segment_align: 8
    .kernarg_segment_size: 84
    .language:       OpenCL C
    .language_version:
      - 2
      - 0
    .max_flat_workgroup_size: 256
    .name:           _Z11agg1_kernelPKDF16_PKfS2_PKiS4_S2_S2_PDF16_PfS6_i
    .private_segment_fixed_size: 0
    .sgpr_count:     54
    .sgpr_spill_count: 0
    .symbol:         _Z11agg1_kernelPKDF16_PKfS2_PKiS4_S2_S2_PDF16_PfS6_i.kd
    .uniform_work_group_size: 1
    .uses_dynamic_stack: false
    .vgpr_count:     70
    .vgpr_spill_count: 0
    .wavefront_size: 64
  - .agpr_count:     0
    .args:
      - .actual_access:  read_only
        .address_space:  global
        .offset:         0
        .size:           8
        .value_kind:     global_buffer
      - .actual_access:  read_only
        .address_space:  global
        .offset:         8
        .size:           8
        .value_kind:     global_buffer
      - .actual_access:  read_only
        .address_space:  global
        .offset:         16
        .size:           8
        .value_kind:     global_buffer
      - .actual_access:  read_only
        .address_space:  global
        .offset:         24
        .size:           8
        .value_kind:     global_buffer
      - .actual_access:  read_only
        .address_space:  global
        .offset:         32
        .size:           8
        .value_kind:     global_buffer
      - .actual_access:  write_only
        .address_space:  global
        .offset:         40
        .size:           8
        .value_kind:     global_buffer
      - .offset:         48
        .size:           4
        .value_kind:     by_value
    .group_segment_fixed_size: 0
    .kernarg_segment_align: 8
    .kernarg_segment_size: 52
    .language:       OpenCL C
    .language_version:
      - 2
      - 0
    .max_flat_workgroup_size: 256
    .name:           _Z13stats2_kernelPKiS0_PKfS2_S0_P15HIP_vector_typeIfLj4EEi
    .private_segment_fixed_size: 0
    .sgpr_count:     38
    .sgpr_spill_count: 0
    .symbol:         _Z13stats2_kernelPKiS0_PKfS2_S0_P15HIP_vector_typeIfLj4EEi.kd
    .uniform_work_group_size: 1
    .uses_dynamic_stack: false
    .vgpr_count:     32
    .vgpr_spill_count: 0
    .wavefront_size: 64
  - .agpr_count:     0
    .args:
      - .actual_access:  read_only
        .address_space:  global
        .offset:         0
        .size:           8
        .value_kind:     global_buffer
      - .actual_access:  read_only
        .address_space:  global
        .offset:         8
        .size:           8
        .value_kind:     global_buffer
      - .actual_access:  read_only
        .address_space:  global
        .offset:         16
        .size:           8
        .value_kind:     global_buffer
      - .actual_access:  read_only
        .address_space:  global
        .offset:         24
        .size:           8
        .value_kind:     global_buffer
      - .actual_access:  read_only
        .address_space:  global
        .offset:         32
        .size:           8
        .value_kind:     global_buffer
      - .actual_access:  write_only
        .address_space:  global
        .offset:         40
        .size:           8
        .value_kind:     global_buffer
      - .offset:         48
        .size:           4
        .value_kind:     by_value
    .group_segment_fixed_size: 70752
    .kernarg_segment_align: 8
    .kernarg_segment_size: 52
    .language:       OpenCL C
    .language_version:
      - 2
      - 0
    .max_flat_workgroup_size: 1024
    .name:           _Z12pool2_kernelPKjPKiPKfPK15HIP_vector_typeIfLj4EEPKDF16_Pfi
    .private_segment_fixed_size: 0
    .sgpr_count:     26
    .sgpr_spill_count: 0
    .symbol:         _Z12pool2_kernelPKjPKiPKfPK15HIP_vector_typeIfLj4EEPKDF16_Pfi.kd
    .uniform_work_group_size: 1
    .uses_dynamic_stack: false
    .vgpr_count:     128
    .vgpr_spill_count: 0
    .wavefront_size: 64
  - .agpr_count:     0
    .args:
      - .actual_access:  read_only
        .address_space:  global
        .offset:         0
        .size:           8
        .value_kind:     global_buffer
      - .actual_access:  read_only
        .address_space:  global
        .offset:         8
        .size:           8
        .value_kind:     global_buffer
      - .actual_access:  read_only
        .address_space:  global
        .offset:         16
        .size:           8
        .value_kind:     global_buffer
      - .actual_access:  read_only
        .address_space:  global
        .offset:         24
        .size:           8
        .value_kind:     global_buffer
      - .actual_access:  read_only
        .address_space:  global
        .offset:         32
        .size:           8
        .value_kind:     global_buffer
      - .actual_access:  read_only
        .address_space:  global
        .offset:         40
        .size:           8
        .value_kind:     global_buffer
      - .actual_access:  read_only
        .address_space:  global
        .offset:         48
        .size:           8
        .value_kind:     global_buffer
      - .actual_access:  read_only
        .address_space:  global
        .offset:         56
        .size:           8
        .value_kind:     global_buffer
      - .actual_access:  write_only
        .address_space:  global
        .offset:         64
        .size:           8
        .value_kind:     global_buffer
    .group_segment_fixed_size: 9472
    .kernarg_segment_align: 8
    .kernarg_segment_size: 72
    .language:       OpenCL C
    .language_version:
      - 2
      - 0
    .max_flat_workgroup_size: 1024
    .name:           _Z10mlp_kernelPKfPKiS0_S0_S0_S0_S0_S0_Pf
    .private_segment_fixed_size: 0
    .sgpr_count:     76
    .sgpr_spill_count: 0
    .symbol:         _Z10mlp_kernelPKfPKiS0_S0_S0_S0_S0_S0_Pf.kd
    .uniform_work_group_size: 1
    .uses_dynamic_stack: false
    .vgpr_count:     77
    .vgpr_spill_count: 0
    .wavefront_size: 64
